# in-projection epilogue: non-temporal stores for the 579 MB projection buffer so that it does not displace the GEMM operands in L2
# speedup vs baseline: 1.0074x; 1.0074x over previous
.LBB0_194:
	v_lshl_or_b32 v20, s28, 8, v190
	v_cvt_pk_bf16_f32 v26, v26, v27
	v_cvt_pk_bf16_f32 v27, v22, v23
	v_mov_b64_e32 v[22:23], s[96:97]
	v_ashrrev_i32_e32 v21, 31, v20
	v_mad_i64_i32 v[22:23], s[30:31], v18, s51, v[22:23]
	v_cvt_pk_bf16_f32 v28, v28, v29
	v_cvt_pk_bf16_f32 v29, v24, v25
	v_lshl_add_u64 v[22:23], v[20:21], 1, v[22:23]
	global_store_dwordx4 v[22:23], v[26:29], off nt
	v_pk_mul_f32 v[24:25], v[152:153], s[18:19] op_sel_hi:[1,0]
	s_and_b64 vcc, exec, s[6:7]
	v_pk_mul_f32 v[28:29], v[150:151], s[18:19] op_sel_hi:[1,0]
	v_pk_mul_f32 v[26:27], v[148:149], s[18:19] op_sel_hi:[1,0]
	v_pk_mul_f32 v[30:31], v[146:147], s[18:19] op_sel_hi:[1,0]
	s_cbranch_vccnz .LBB0_196
	v_and_b32_e32 v19, 64, v195
	v_xor_b32_e32 v0, 32, v195
	v_add_u32_e32 v19, 64, v19
	v_cmp_lt_i32_e32 vcc, v0, v19
	s_waitcnt vmcnt(0)
	v_pk_mul_f32 v[14:15], v[28:29], v[14:15]
	v_mul_f32_e32 v16, v24, v16
	v_cndmask_b32_e32 v0, v195, v0, vcc
	v_lshlrev_b32_e32 v0, 2, v0
	ds_bpermute_b32 v32, v0, v28
	ds_bpermute_b32 v33, v0, v29
	ds_bpermute_b32 v19, v0, v24
	ds_bpermute_b32 v146, v0, v30
	ds_bpermute_b32 v147, v0, v31
	v_mul_f32_e32 v4, v26, v4
	s_waitcnt lgkmcnt(3)
	v_pk_mul_f32 v[28:29], v[170:171], v[32:33]
	ds_bpermute_b32 v32, v0, v26
	s_waitcnt lgkmcnt(3)
	v_mul_f32_e32 v19, v170, v19
	v_mul_f32_e32 v24, v12, v19
	ds_bpermute_b32 v12, v0, v25
	ds_bpermute_b32 v0, v0, v27
	s_waitcnt lgkmcnt(2)
	v_mul_f32_e32 v19, v170, v32
	v_mul_f32_e32 v26, v8, v19
	v_mov_b32_e32 v32, v17
	s_waitcnt lgkmcnt(1)
	v_mul_f32_e32 v33, v170, v12
	v_mov_b32_e32 v12, v25
	v_pk_fma_f32 v[28:29], v[10:11], v[28:29], v[14:15]
	s_waitcnt lgkmcnt(0)
	v_mul_f32_e32 v11, v170, v0
	v_mov_b32_e32 v8, v27
	v_mov_b32_e32 v10, v5
	v_pk_mul_f32 v[12:13], v[12:13], v[32:33]
	v_pk_mul_f32 v[8:9], v[8:9], v[10:11]
	v_pk_mul_f32 v[2:3], v[30:31], v[2:3]
	v_pk_mul_f32 v[30:31], v[170:171], v[146:147]
	v_mov_b32_e32 v17, v12
	v_mov_b32_e32 v25, v13
	v_mov_b32_e32 v5, v8
	v_mov_b32_e32 v27, v9
	v_pk_add_f32 v[24:25], v[16:17], v[24:25]
	v_pk_fma_f32 v[30:31], v[6:7], v[30:31], v[2:3]
	v_pk_add_f32 v[26:27], v[4:5], v[26:27]
.LBB0_196:
	v_cvt_pk_bf16_f32 v2, v28, v29
	v_cvt_pk_bf16_f32 v3, v24, v25
	v_cvt_pk_bf16_f32 v4, v30, v31
	v_cvt_pk_bf16_f32 v5, v26, v27
	global_store_dwordx4 v[22:23], v[2:5], off offset:256 nt
	v_or_b32_e32 v22, 16, v18
	s_and_b64 vcc, exec, s[6:7]
	v_ashrrev_i32_e32 v23, 31, v22
	s_cbranch_vccnz .LBB0_198
	v_lshlrev_b64 v[2:3], 6, v[22:23]
	v_lshl_add_u64 v[6:7], v[172:173], 0, v[2:3]
	v_lshl_add_u64 v[8:9], v[174:175], 0, v[2:3]
	global_load_dwordx4 v[2:5], v[6:7], off offset:16
	global_load_dwordx4 v[14:17], v[6:7], off
	global_load_dwordx4 v[10:13], v[8:9], off
	s_nop 0
	global_load_dwordx4 v[6:9], v[8:9], off offset:16
	s_branch .LBB0_199

.LBB0_201:
	v_cvt_pk_bf16_f32 v28, v28, v29
	v_cvt_pk_bf16_f32 v29, v24, v25
	v_mov_b64_e32 v[24:25], s[96:97]
	v_mad_i64_i32 v[22:23], s[30:31], v22, s51, v[24:25]
	v_cvt_pk_bf16_f32 v30, v30, v31
	v_cvt_pk_bf16_f32 v31, v26, v27
	v_lshl_add_u64 v[22:23], v[20:21], 1, v[22:23]
	global_store_dwordx4 v[22:23], v[28:31], off nt
	v_pk_mul_f32 v[24:25], v[136:137], s[18:19] op_sel_hi:[1,0]
	v_pk_mul_f32 v[26:27], v[132:133], s[18:19] op_sel_hi:[1,0]
	v_pk_mul_f32 v[28:29], v[134:135], s[18:19] op_sel_hi:[1,0]
	s_and_b64 vcc, exec, s[6:7]
	v_pk_mul_f32 v[30:31], v[130:131], s[18:19] op_sel_hi:[1,0]
	s_cbranch_vccnz .LBB0_203
	v_and_b32_e32 v19, 64, v195
	v_xor_b32_e32 v0, 32, v195
	v_add_u32_e32 v19, 64, v19
	v_cmp_lt_i32_e32 vcc, v0, v19
	s_waitcnt vmcnt(3)
	v_pk_mul_f32 v[14:15], v[28:29], v[14:15]
	v_mul_f32_e32 v16, v24, v16
	v_cndmask_b32_e32 v0, v195, v0, vcc
	v_lshlrev_b32_e32 v0, 2, v0
	ds_bpermute_b32 v32, v0, v28
	ds_bpermute_b32 v33, v0, v29
	ds_bpermute_b32 v19, v0, v24
	ds_bpermute_b32 v130, v0, v30
	ds_bpermute_b32 v131, v0, v31
	v_mul_f32_e32 v4, v26, v4
	s_waitcnt lgkmcnt(3)
	v_pk_mul_f32 v[28:29], v[170:171], v[32:33]
	ds_bpermute_b32 v32, v0, v26
	s_waitcnt lgkmcnt(3)
	v_mul_f32_e32 v19, v170, v19
	s_waitcnt vmcnt(2)
	v_mul_f32_e32 v24, v12, v19
	ds_bpermute_b32 v12, v0, v25
	ds_bpermute_b32 v0, v0, v27
	s_waitcnt lgkmcnt(2)
	v_mul_f32_e32 v19, v170, v32
	s_waitcnt vmcnt(1)
	v_mul_f32_e32 v26, v8, v19
	v_mov_b32_e32 v32, v17
	s_waitcnt lgkmcnt(1)
	v_mul_f32_e32 v33, v170, v12
	v_mov_b32_e32 v12, v25
	v_pk_fma_f32 v[28:29], v[10:11], v[28:29], v[14:15]
	s_waitcnt lgkmcnt(0)
	v_mul_f32_e32 v11, v170, v0
	v_mov_b32_e32 v8, v27
	v_mov_b32_e32 v10, v5
	v_pk_mul_f32 v[12:13], v[12:13], v[32:33]
	v_pk_mul_f32 v[8:9], v[8:9], v[10:11]
	v_pk_mul_f32 v[2:3], v[30:31], v[2:3]
	v_pk_mul_f32 v[30:31], v[170:171], v[130:131]
	v_mov_b32_e32 v17, v12
	v_mov_b32_e32 v25, v13
	v_mov_b32_e32 v5, v8
	v_mov_b32_e32 v27, v9
	v_pk_add_f32 v[24:25], v[16:17], v[24:25]
	v_pk_fma_f32 v[30:31], v[6:7], v[30:31], v[2:3]
	v_pk_add_f32 v[26:27], v[4:5], v[26:27]
.LBB0_203:
	v_cvt_pk_bf16_f32 v2, v28, v29
	v_cvt_pk_bf16_f32 v3, v24, v25
	v_cvt_pk_bf16_f32 v4, v30, v31
	v_cvt_pk_bf16_f32 v5, v26, v27
	global_store_dwordx4 v[22:23], v[2:5], off offset:256 nt
	v_or_b32_e32 v22, 32, v18
	s_and_b64 vcc, exec, s[6:7]
	v_ashrrev_i32_e32 v23, 31, v22
	s_cbranch_vccnz .LBB0_205
	v_lshlrev_b64 v[2:3], 6, v[22:23]
	s_waitcnt vmcnt(2)
	v_lshl_add_u64 v[6:7], v[172:173], 0, v[2:3]
	v_lshl_add_u64 v[8:9], v[174:175], 0, v[2:3]
	global_load_dwordx4 v[2:5], v[6:7], off offset:16
	global_load_dwordx4 v[14:17], v[6:7], off
	global_load_dwordx4 v[10:13], v[8:9], off
	s_nop 0
	global_load_dwordx4 v[6:9], v[8:9], off offset:16
	s_branch .LBB0_206

.LBB0_208:
	v_cvt_pk_bf16_f32 v28, v28, v29
	v_cvt_pk_bf16_f32 v29, v24, v25
	v_mov_b64_e32 v[24:25], s[96:97]
	v_mad_i64_i32 v[22:23], s[30:31], v22, s51, v[24:25]
	v_cvt_pk_bf16_f32 v30, v30, v31
	v_cvt_pk_bf16_f32 v31, v26, v27
	v_lshl_add_u64 v[22:23], v[20:21], 1, v[22:23]
	global_store_dwordx4 v[22:23], v[28:31], off nt
	v_pk_mul_f32 v[24:25], v[120:121], s[18:19] op_sel_hi:[1,0]
	v_pk_mul_f32 v[26:27], v[116:117], s[18:19] op_sel_hi:[1,0]
	v_pk_mul_f32 v[28:29], v[118:119], s[18:19] op_sel_hi:[1,0]
	s_and_b64 vcc, exec, s[6:7]
	v_pk_mul_f32 v[30:31], v[114:115], s[18:19] op_sel_hi:[1,0]
	s_cbranch_vccnz .LBB0_210
	v_and_b32_e32 v19, 64, v195
	v_xor_b32_e32 v0, 32, v195
	v_add_u32_e32 v19, 64, v19
	v_cmp_lt_i32_e32 vcc, v0, v19
	s_waitcnt vmcnt(3)
	v_pk_mul_f32 v[14:15], v[28:29], v[14:15]
	v_mul_f32_e32 v16, v24, v16
	v_cndmask_b32_e32 v0, v195, v0, vcc
	v_lshlrev_b32_e32 v0, 2, v0
	ds_bpermute_b32 v32, v0, v28
	ds_bpermute_b32 v33, v0, v29
	ds_bpermute_b32 v19, v0, v24
	ds_bpermute_b32 v114, v0, v30
	ds_bpermute_b32 v115, v0, v31
	v_mul_f32_e32 v4, v26, v4
	s_waitcnt lgkmcnt(3)
	v_pk_mul_f32 v[28:29], v[170:171], v[32:33]
	ds_bpermute_b32 v32, v0, v26
	s_waitcnt lgkmcnt(3)
	v_mul_f32_e32 v19, v170, v19
	s_waitcnt vmcnt(2)
	v_mul_f32_e32 v24, v12, v19
	ds_bpermute_b32 v12, v0, v25
	ds_bpermute_b32 v0, v0, v27
	s_waitcnt lgkmcnt(2)
	v_mul_f32_e32 v19, v170, v32
	s_waitcnt vmcnt(1)
	v_mul_f32_e32 v26, v8, v19
	v_mov_b32_e32 v32, v17
	s_waitcnt lgkmcnt(1)
	v_mul_f32_e32 v33, v170, v12
	v_mov_b32_e32 v12, v25
	v_pk_fma_f32 v[28:29], v[10:11], v[28:29], v[14:15]
	s_waitcnt lgkmcnt(0)
	v_mul_f32_e32 v11, v170, v0
	v_mov_b32_e32 v8, v27
	v_mov_b32_e32 v10, v5
	v_pk_mul_f32 v[12:13], v[12:13], v[32:33]
	v_pk_mul_f32 v[8:9], v[8:9], v[10:11]
	v_pk_mul_f32 v[2:3], v[30:31], v[2:3]
	v_pk_mul_f32 v[30:31], v[170:171], v[114:115]
	v_mov_b32_e32 v17, v12
	v_mov_b32_e32 v25, v13
	v_mov_b32_e32 v5, v8
	v_mov_b32_e32 v27, v9
	v_pk_add_f32 v[24:25], v[16:17], v[24:25]
	v_pk_fma_f32 v[30:31], v[6:7], v[30:31], v[2:3]
	v_pk_add_f32 v[26:27], v[4:5], v[26:27]
.LBB0_210:
	v_cvt_pk_bf16_f32 v2, v28, v29
	v_cvt_pk_bf16_f32 v3, v24, v25
	v_cvt_pk_bf16_f32 v4, v30, v31
	v_cvt_pk_bf16_f32 v5, v26, v27
	global_store_dwordx4 v[22:23], v[2:5], off offset:256 nt
	v_or_b32_e32 v22, 48, v18
	s_and_b64 vcc, exec, s[6:7]
	v_ashrrev_i32_e32 v23, 31, v22
	s_cbranch_vccnz .LBB0_212
	v_lshlrev_b64 v[2:3], 6, v[22:23]
	s_waitcnt vmcnt(2)
	v_lshl_add_u64 v[6:7], v[172:173], 0, v[2:3]
	v_lshl_add_u64 v[8:9], v[174:175], 0, v[2:3]
	global_load_dwordx4 v[2:5], v[6:7], off offset:16
	global_load_dwordx4 v[14:17], v[6:7], off
	global_load_dwordx4 v[10:13], v[8:9], off
	s_nop 0
	global_load_dwordx4 v[6:9], v[8:9], off offset:16
	s_branch .LBB0_213

.LBB0_215:
	v_cvt_pk_bf16_f32 v28, v28, v29
	v_cvt_pk_bf16_f32 v29, v24, v25
	v_mov_b64_e32 v[24:25], s[96:97]
	v_mad_i64_i32 v[22:23], s[30:31], v22, s51, v[24:25]
	v_cvt_pk_bf16_f32 v30, v30, v31
	v_cvt_pk_bf16_f32 v31, v26, v27
	v_lshl_add_u64 v[22:23], v[20:21], 1, v[22:23]
	global_store_dwordx4 v[22:23], v[28:31], off nt
	v_pk_mul_f32 v[24:25], v[104:105], s[18:19] op_sel_hi:[1,0]
	v_pk_mul_f32 v[26:27], v[100:101], s[18:19] op_sel_hi:[1,0]
	v_pk_mul_f32 v[28:29], v[102:103], s[18:19] op_sel_hi:[1,0]
	s_and_b64 vcc, exec, s[6:7]
	v_pk_mul_f32 v[30:31], v[98:99], s[18:19] op_sel_hi:[1,0]
	s_cbranch_vccnz .LBB0_217
	v_and_b32_e32 v19, 64, v195
	v_xor_b32_e32 v0, 32, v195
	v_add_u32_e32 v19, 64, v19
	v_cmp_lt_i32_e32 vcc, v0, v19
	s_waitcnt vmcnt(3)
	v_pk_mul_f32 v[14:15], v[28:29], v[14:15]
	v_mul_f32_e32 v16, v24, v16
	v_cndmask_b32_e32 v0, v195, v0, vcc
	v_lshlrev_b32_e32 v0, 2, v0
	ds_bpermute_b32 v32, v0, v28
	ds_bpermute_b32 v33, v0, v29
	ds_bpermute_b32 v19, v0, v24
	ds_bpermute_b32 v98, v0, v30
	ds_bpermute_b32 v99, v0, v31
	v_mul_f32_e32 v4, v26, v4
	s_waitcnt lgkmcnt(3)
	v_pk_mul_f32 v[28:29], v[170:171], v[32:33]
	ds_bpermute_b32 v32, v0, v26
	s_waitcnt lgkmcnt(3)
	v_mul_f32_e32 v19, v170, v19
	s_waitcnt vmcnt(2)
	v_mul_f32_e32 v24, v12, v19
	ds_bpermute_b32 v12, v0, v25
	ds_bpermute_b32 v0, v0, v27
	s_waitcnt lgkmcnt(2)
	v_mul_f32_e32 v19, v170, v32
	s_waitcnt vmcnt(1)
	v_mul_f32_e32 v26, v8, v19
	v_mov_b32_e32 v32, v17
	s_waitcnt lgkmcnt(1)
	v_mul_f32_e32 v33, v170, v12
	v_mov_b32_e32 v12, v25
	v_pk_fma_f32 v[28:29], v[10:11], v[28:29], v[14:15]
	s_waitcnt lgkmcnt(0)
	v_mul_f32_e32 v11, v170, v0
	v_mov_b32_e32 v8, v27
	v_mov_b32_e32 v10, v5
	v_pk_mul_f32 v[12:13], v[12:13], v[32:33]
	v_pk_mul_f32 v[8:9], v[8:9], v[10:11]
	v_pk_mul_f32 v[2:3], v[30:31], v[2:3]
	v_pk_mul_f32 v[30:31], v[170:171], v[98:99]
	v_mov_b32_e32 v17, v12
	v_mov_b32_e32 v25, v13
	v_mov_b32_e32 v5, v8
	v_mov_b32_e32 v27, v9
	v_pk_add_f32 v[24:25], v[16:17], v[24:25]
	v_pk_fma_f32 v[30:31], v[6:7], v[30:31], v[2:3]
	v_pk_add_f32 v[26:27], v[4:5], v[26:27]
.LBB0_217:
	v_cvt_pk_bf16_f32 v2, v28, v29
	v_cvt_pk_bf16_f32 v3, v24, v25
	v_cvt_pk_bf16_f32 v4, v30, v31
	v_cvt_pk_bf16_f32 v5, v26, v27
	global_store_dwordx4 v[22:23], v[2:5], off offset:256 nt
	v_add_u32_e32 v22, 0x80, v18
	s_and_b64 vcc, exec, s[6:7]
	v_ashrrev_i32_e32 v23, 31, v22
	s_cbranch_vccnz .LBB0_219
	v_lshlrev_b64 v[2:3], 6, v[22:23]
	s_waitcnt vmcnt(2)
	v_lshl_add_u64 v[6:7], v[172:173], 0, v[2:3]
	v_lshl_add_u64 v[8:9], v[174:175], 0, v[2:3]
	global_load_dwordx4 v[2:5], v[6:7], off offset:16
	global_load_dwordx4 v[14:17], v[6:7], off
	global_load_dwordx4 v[10:13], v[8:9], off
	s_nop 0
	global_load_dwordx4 v[6:9], v[8:9], off offset:16
	s_branch .LBB0_220

.LBB0_222:
	v_cvt_pk_bf16_f32 v28, v28, v29
	v_cvt_pk_bf16_f32 v29, v24, v25
	v_mov_b64_e32 v[24:25], s[96:97]
	v_mad_i64_i32 v[22:23], s[30:31], v22, s51, v[24:25]
	v_cvt_pk_bf16_f32 v30, v30, v31
	v_cvt_pk_bf16_f32 v31, v26, v27
	v_lshl_add_u64 v[22:23], v[20:21], 1, v[22:23]
	global_store_dwordx4 v[22:23], v[28:31], off nt
	v_pk_mul_f32 v[24:25], v[88:89], s[18:19] op_sel_hi:[1,0]
	v_pk_mul_f32 v[26:27], v[84:85], s[18:19] op_sel_hi:[1,0]
	v_pk_mul_f32 v[28:29], v[86:87], s[18:19] op_sel_hi:[1,0]
	s_and_b64 vcc, exec, s[6:7]
	v_pk_mul_f32 v[30:31], v[82:83], s[18:19] op_sel_hi:[1,0]
	s_cbranch_vccnz .LBB0_224
	v_and_b32_e32 v19, 64, v195
	v_xor_b32_e32 v0, 32, v195
	v_add_u32_e32 v19, 64, v19
	v_cmp_lt_i32_e32 vcc, v0, v19
	s_waitcnt vmcnt(3)
	v_pk_mul_f32 v[14:15], v[28:29], v[14:15]
	v_mul_f32_e32 v16, v24, v16
	v_cndmask_b32_e32 v0, v195, v0, vcc
	v_lshlrev_b32_e32 v0, 2, v0
	ds_bpermute_b32 v32, v0, v28
	ds_bpermute_b32 v33, v0, v29
	ds_bpermute_b32 v19, v0, v24
	ds_bpermute_b32 v82, v0, v30
	ds_bpermute_b32 v83, v0, v31
	v_mul_f32_e32 v4, v26, v4
	s_waitcnt lgkmcnt(3)
	v_pk_mul_f32 v[28:29], v[170:171], v[32:33]
	ds_bpermute_b32 v32, v0, v26
	s_waitcnt lgkmcnt(3)
	v_mul_f32_e32 v19, v170, v19
	s_waitcnt vmcnt(2)
	v_mul_f32_e32 v24, v12, v19
	ds_bpermute_b32 v12, v0, v25
	ds_bpermute_b32 v0, v0, v27
	s_waitcnt lgkmcnt(2)
	v_mul_f32_e32 v19, v170, v32
	s_waitcnt vmcnt(1)
	v_mul_f32_e32 v26, v8, v19
	v_mov_b32_e32 v32, v17
	s_waitcnt lgkmcnt(1)
	v_mul_f32_e32 v33, v170, v12
	v_mov_b32_e32 v12, v25
	v_pk_fma_f32 v[28:29], v[10:11], v[28:29], v[14:15]
	s_waitcnt lgkmcnt(0)
	v_mul_f32_e32 v11, v170, v0
	v_mov_b32_e32 v8, v27
	v_mov_b32_e32 v10, v5
	v_pk_mul_f32 v[12:13], v[12:13], v[32:33]
	v_pk_mul_f32 v[8:9], v[8:9], v[10:11]
	v_pk_mul_f32 v[2:3], v[30:31], v[2:3]
	v_pk_mul_f32 v[30:31], v[170:171], v[82:83]
	v_mov_b32_e32 v17, v12
	v_mov_b32_e32 v25, v13
	v_mov_b32_e32 v5, v8
	v_mov_b32_e32 v27, v9
	v_pk_add_f32 v[24:25], v[16:17], v[24:25]
	v_pk_fma_f32 v[30:31], v[6:7], v[30:31], v[2:3]
	v_pk_add_f32 v[26:27], v[4:5], v[26:27]
.LBB0_224:
	v_cvt_pk_bf16_f32 v2, v28, v29
	v_cvt_pk_bf16_f32 v3, v24, v25
	v_cvt_pk_bf16_f32 v4, v30, v31
	v_cvt_pk_bf16_f32 v5, v26, v27
	global_store_dwordx4 v[22:23], v[2:5], off offset:256 nt
	v_add_u32_e32 v22, 0x90, v18
	s_and_b64 vcc, exec, s[6:7]
	v_ashrrev_i32_e32 v23, 31, v22
	s_cbranch_vccnz .LBB0_226
	v_lshlrev_b64 v[2:3], 6, v[22:23]
	s_waitcnt vmcnt(2)
	v_lshl_add_u64 v[6:7], v[172:173], 0, v[2:3]
	v_lshl_add_u64 v[8:9], v[174:175], 0, v[2:3]
	global_load_dwordx4 v[2:5], v[6:7], off offset:16
	global_load_dwordx4 v[14:17], v[6:7], off
	global_load_dwordx4 v[10:13], v[8:9], off
	s_nop 0
	global_load_dwordx4 v[6:9], v[8:9], off offset:16
	s_branch .LBB0_227

.LBB0_229:
	v_cvt_pk_bf16_f32 v28, v28, v29
	v_cvt_pk_bf16_f32 v29, v24, v25
	v_mov_b64_e32 v[24:25], s[96:97]
	v_mad_i64_i32 v[22:23], s[30:31], v22, s51, v[24:25]
	v_cvt_pk_bf16_f32 v30, v30, v31
	v_cvt_pk_bf16_f32 v31, v26, v27
	v_lshl_add_u64 v[22:23], v[20:21], 1, v[22:23]
	global_store_dwordx4 v[22:23], v[28:31], off nt
	v_pk_mul_f32 v[24:25], v[72:73], s[18:19] op_sel_hi:[1,0]
	v_pk_mul_f32 v[26:27], v[68:69], s[18:19] op_sel_hi:[1,0]
	v_pk_mul_f32 v[28:29], v[70:71], s[18:19] op_sel_hi:[1,0]
	s_and_b64 vcc, exec, s[6:7]
	v_pk_mul_f32 v[30:31], v[66:67], s[18:19] op_sel_hi:[1,0]
	s_cbranch_vccnz .LBB0_231
	v_and_b32_e32 v19, 64, v195
	v_xor_b32_e32 v0, 32, v195
	v_add_u32_e32 v19, 64, v19
	v_cmp_lt_i32_e32 vcc, v0, v19
	s_waitcnt vmcnt(3)
	v_pk_mul_f32 v[14:15], v[28:29], v[14:15]
	v_mul_f32_e32 v16, v24, v16
	v_cndmask_b32_e32 v0, v195, v0, vcc
	v_lshlrev_b32_e32 v0, 2, v0
	ds_bpermute_b32 v32, v0, v28
	ds_bpermute_b32 v33, v0, v29
	ds_bpermute_b32 v19, v0, v24
	ds_bpermute_b32 v66, v0, v30
	ds_bpermute_b32 v67, v0, v31
	v_mul_f32_e32 v4, v26, v4
	s_waitcnt lgkmcnt(3)
	v_pk_mul_f32 v[28:29], v[170:171], v[32:33]
	ds_bpermute_b32 v32, v0, v26
	s_waitcnt lgkmcnt(3)
	v_mul_f32_e32 v19, v170, v19
	s_waitcnt vmcnt(2)
	v_mul_f32_e32 v24, v12, v19
	ds_bpermute_b32 v12, v0, v25
	ds_bpermute_b32 v0, v0, v27
	s_waitcnt lgkmcnt(2)
	v_mul_f32_e32 v19, v170, v32
	s_waitcnt vmcnt(1)
	v_mul_f32_e32 v26, v8, v19
	v_mov_b32_e32 v32, v17
	s_waitcnt lgkmcnt(1)
	v_mul_f32_e32 v33, v170, v12
	v_mov_b32_e32 v12, v25
	v_pk_fma_f32 v[28:29], v[10:11], v[28:29], v[14:15]
	s_waitcnt lgkmcnt(0)
	v_mul_f32_e32 v11, v170, v0
	v_mov_b32_e32 v8, v27
	v_mov_b32_e32 v10, v5
	v_pk_mul_f32 v[12:13], v[12:13], v[32:33]
	v_pk_mul_f32 v[8:9], v[8:9], v[10:11]
	v_pk_mul_f32 v[2:3], v[30:31], v[2:3]
	v_pk_mul_f32 v[30:31], v[170:171], v[66:67]
	v_mov_b32_e32 v17, v12
	v_mov_b32_e32 v25, v13
	v_mov_b32_e32 v5, v8
	v_mov_b32_e32 v27, v9
	v_pk_add_f32 v[24:25], v[16:17], v[24:25]
	v_pk_fma_f32 v[30:31], v[6:7], v[30:31], v[2:3]
	v_pk_add_f32 v[26:27], v[4:5], v[26:27]
.LBB0_231:
	v_cvt_pk_bf16_f32 v2, v28, v29
	v_cvt_pk_bf16_f32 v3, v24, v25
	v_cvt_pk_bf16_f32 v4, v30, v31
	v_cvt_pk_bf16_f32 v5, v26, v27
	global_store_dwordx4 v[22:23], v[2:5], off offset:256 nt
	v_add_u32_e32 v22, 0xa0, v18
	s_and_b64 vcc, exec, s[6:7]
	v_ashrrev_i32_e32 v23, 31, v22
	s_cbranch_vccnz .LBB0_233
	v_lshlrev_b64 v[2:3], 6, v[22:23]
	s_waitcnt vmcnt(2)
	v_lshl_add_u64 v[6:7], v[172:173], 0, v[2:3]
	v_lshl_add_u64 v[8:9], v[174:175], 0, v[2:3]
	global_load_dwordx4 v[2:5], v[6:7], off offset:16
	global_load_dwordx4 v[14:17], v[6:7], off
	global_load_dwordx4 v[10:13], v[8:9], off
	s_nop 0
	global_load_dwordx4 v[6:9], v[8:9], off offset:16
	s_branch .LBB0_234

.LBB0_236:
	v_cvt_pk_bf16_f32 v28, v28, v29
	v_cvt_pk_bf16_f32 v29, v24, v25
	v_mov_b64_e32 v[24:25], s[96:97]
	v_mad_i64_i32 v[22:23], s[30:31], v22, s51, v[24:25]
	v_cvt_pk_bf16_f32 v30, v30, v31
	v_cvt_pk_bf16_f32 v31, v26, v27
	v_lshl_add_u64 v[22:23], v[20:21], 1, v[22:23]
	global_store_dwordx4 v[22:23], v[28:31], off nt
	v_pk_mul_f32 v[24:25], v[56:57], s[18:19] op_sel_hi:[1,0]
	v_pk_mul_f32 v[26:27], v[52:53], s[18:19] op_sel_hi:[1,0]
	v_pk_mul_f32 v[28:29], v[54:55], s[18:19] op_sel_hi:[1,0]
	s_and_b64 vcc, exec, s[6:7]
	v_pk_mul_f32 v[30:31], v[50:51], s[18:19] op_sel_hi:[1,0]
	s_cbranch_vccnz .LBB0_238
	v_and_b32_e32 v19, 64, v195
	v_xor_b32_e32 v0, 32, v195
	v_add_u32_e32 v19, 64, v19
	v_cmp_lt_i32_e32 vcc, v0, v19
	s_waitcnt vmcnt(3)
	v_pk_mul_f32 v[14:15], v[28:29], v[14:15]
	v_mul_f32_e32 v16, v24, v16
	v_cndmask_b32_e32 v0, v195, v0, vcc
	v_lshlrev_b32_e32 v0, 2, v0
	ds_bpermute_b32 v32, v0, v28
	ds_bpermute_b32 v33, v0, v29
	ds_bpermute_b32 v19, v0, v24
	ds_bpermute_b32 v50, v0, v30
	ds_bpermute_b32 v51, v0, v31
	v_mul_f32_e32 v4, v26, v4
	s_waitcnt lgkmcnt(3)
	v_pk_mul_f32 v[28:29], v[170:171], v[32:33]
	ds_bpermute_b32 v32, v0, v26
	s_waitcnt lgkmcnt(3)
	v_mul_f32_e32 v19, v170, v19
	s_waitcnt vmcnt(2)
	v_mul_f32_e32 v24, v12, v19
	ds_bpermute_b32 v12, v0, v25
	ds_bpermute_b32 v0, v0, v27
	s_waitcnt lgkmcnt(2)
	v_mul_f32_e32 v19, v170, v32
	s_waitcnt vmcnt(1)
	v_mul_f32_e32 v26, v8, v19
	v_mov_b32_e32 v32, v17
	s_waitcnt lgkmcnt(1)
	v_mul_f32_e32 v33, v170, v12
	v_mov_b32_e32 v12, v25
	v_pk_fma_f32 v[28:29], v[10:11], v[28:29], v[14:15]
	s_waitcnt lgkmcnt(0)
	v_mul_f32_e32 v11, v170, v0
	v_mov_b32_e32 v8, v27
	v_mov_b32_e32 v10, v5
	v_pk_mul_f32 v[12:13], v[12:13], v[32:33]
	v_pk_mul_f32 v[8:9], v[8:9], v[10:11]
	v_pk_mul_f32 v[2:3], v[30:31], v[2:3]
	v_pk_mul_f32 v[30:31], v[170:171], v[50:51]
	v_mov_b32_e32 v17, v12
	v_mov_b32_e32 v25, v13
	v_mov_b32_e32 v5, v8
	v_mov_b32_e32 v27, v9
	v_pk_add_f32 v[24:25], v[16:17], v[24:25]
	v_pk_fma_f32 v[30:31], v[6:7], v[30:31], v[2:3]
	v_pk_add_f32 v[26:27], v[4:5], v[26:27]
.LBB0_238:
	v_add_u32_e32 v18, 0xb0, v18
	s_and_b64 vcc, exec, s[6:7]
	v_ashrrev_i32_e32 v19, 31, v18
	v_cvt_pk_bf16_f32 v2, v28, v29
	v_cvt_pk_bf16_f32 v3, v24, v25
	v_cvt_pk_bf16_f32 v4, v30, v31
	v_cvt_pk_bf16_f32 v5, v26, v27
	global_store_dwordx4 v[22:23], v[2:5], off offset:256 nt
	s_cbranch_vccnz .LBB0_240
	s_nop 0
	v_lshlrev_b64 v[2:3], 6, v[18:19]
	s_waitcnt vmcnt(2)
	v_lshl_add_u64 v[6:7], v[172:173], 0, v[2:3]
	v_lshl_add_u64 v[8:9], v[174:175], 0, v[2:3]
	global_load_dwordx4 v[2:5], v[6:7], off offset:16
	global_load_dwordx4 v[14:17], v[6:7], off
	global_load_dwordx4 v[10:13], v[8:9], off
	s_nop 0
	global_load_dwordx4 v[6:9], v[8:9], off offset:16
	s_branch .LBB0_241

.LBB0_243:
	v_cvt_pk_bf16_f32 v26, v26, v27
	v_cvt_pk_bf16_f32 v27, v22, v23
	v_mov_b64_e32 v[22:23], s[96:97]
	v_mad_i64_i32 v[18:19], s[30:31], v18, s51, v[22:23]
	v_lshl_add_u64 v[18:19], v[20:21], 1, v[18:19]
	v_cvt_pk_bf16_f32 v28, v28, v29
	v_cvt_pk_bf16_f32 v29, v24, v25
	global_store_dwordx4 v[18:19], v[26:29], off nt
	v_pk_mul_f32 v[20:21], v[40:41], s[18:19] op_sel_hi:[1,0]
	v_pk_mul_f32 v[24:25], v[38:39], s[18:19] op_sel_hi:[1,0]
	v_pk_mul_f32 v[22:23], v[36:37], s[18:19] op_sel_hi:[1,0]
	s_and_b64 vcc, exec, s[6:7]
	v_pk_mul_f32 v[26:27], v[34:35], s[18:19] op_sel_hi:[1,0]
	s_cbranch_vccnz .LBB0_245
	v_and_b32_e32 v28, 64, v195
	v_xor_b32_e32 v0, 32, v195
	v_add_u32_e32 v28, 64, v28
	v_cmp_lt_i32_e32 vcc, v0, v28
	s_waitcnt vmcnt(3)
	v_pk_mul_f32 v[14:15], v[24:25], v[14:15]
	v_mul_f32_e32 v16, v20, v16
	v_cndmask_b32_e32 v0, v195, v0, vcc
	v_lshlrev_b32_e32 v0, 2, v0
	ds_bpermute_b32 v28, v0, v24
	ds_bpermute_b32 v29, v0, v25
	ds_bpermute_b32 v30, v0, v26
	ds_bpermute_b32 v31, v0, v27
	v_mul_f32_e32 v4, v22, v4
	v_pk_mul_f32 v[2:3], v[26:27], v[2:3]
	s_waitcnt lgkmcnt(2)
	v_pk_mul_f32 v[24:25], v[170:171], v[28:29]
	ds_bpermute_b32 v28, v0, v20
	ds_bpermute_b32 v29, v0, v22
	s_waitcnt vmcnt(2)
	v_pk_fma_f32 v[24:25], v[10:11], v[24:25], v[14:15]
	v_mov_b32_e32 v10, v5
	s_waitcnt lgkmcnt(2)
	v_pk_mul_f32 v[26:27], v[170:171], v[30:31]
	s_waitcnt lgkmcnt(1)
	v_mul_f32_e32 v20, v170, v28
	v_mul_f32_e32 v20, v12, v20
	ds_bpermute_b32 v12, v0, v21
	ds_bpermute_b32 v0, v0, v23
	s_waitcnt lgkmcnt(2)
	v_mul_f32_e32 v22, v170, v29
	s_waitcnt vmcnt(1)
	v_mul_f32_e32 v22, v8, v22
	v_mov_b32_e32 v28, v17
	s_waitcnt lgkmcnt(1)
	v_mul_f32_e32 v29, v170, v12
	v_mov_b32_e32 v12, v21
	s_waitcnt lgkmcnt(0)
	v_mul_f32_e32 v11, v170, v0
	v_mov_b32_e32 v8, v23
	v_pk_mul_f32 v[12:13], v[12:13], v[28:29]
	v_pk_mul_f32 v[8:9], v[8:9], v[10:11]
	v_mov_b32_e32 v17, v12
	v_mov_b32_e32 v21, v13
	v_mov_b32_e32 v5, v8
	v_mov_b32_e32 v23, v9
	v_pk_add_f32 v[20:21], v[16:17], v[20:21]
	v_pk_fma_f32 v[26:27], v[6:7], v[26:27], v[2:3]
	v_pk_add_f32 v[22:23], v[4:5], v[22:23]
.LBB0_245:
	s_andn2_b64 vcc, exec, s[4:5]
	s_mov_b64 s[4:5], -1
	v_cvt_pk_bf16_f32 v2, v24, v25
	v_cvt_pk_bf16_f32 v3, v20, v21
	v_cvt_pk_bf16_f32 v4, v26, v27
	v_cvt_pk_bf16_f32 v5, v22, v23
	global_store_dwordx4 v[18:19], v[2:5], off offset:256 nt
	s_cbranch_vccnz .LBB0_182
	s_andn2_b64 vcc, exec, s[10:11]
	s_cbranch_vccnz .LBB0_181
	s_barrier
	s_branch .LBB0_181
